# in-proj GEMM epilogue: the 8 per-row 1/rms values loaded once at epilogue start instead of one load + full wait per 16-row step
# speedup vs baseline: 1.0822x; 1.0085x over previous
;     __device__ __forceinline__ void operator()(const f32x4 (&acc)[2][2][4][2], const Unit& u, int wr, int wc, int fr, int fq) const {
;         const int row0 = u.pm * BM + wr * 64 + fr, kind = u.pn >> 2;
; #pragma unroll
;         for (int ai = 0; ai < 2; ++ai)
; #pragma unroll
;             for (int m = 0; m < 4; ++m) {
;                 const int row = row0 + ai * HALF + m * 16, pos = row & (MS - 1);
;                 const float rs = rstd[row];
; #pragma unroll
;                 for (int bj = 0; bj < 2; ++bj) {
;                     const int c0 = u.pn * BM + bj * HALF + wc * 32 + 8 * fq;
;                     f32x4 v0 = acc[ai][bj][m][0] * rs, v1 = acc[ai][bj][m][1] * rs;
;                     if (kind <= 1) {
;                         float s = (v0[0] * v0[0] + v0[1] * v0[1]) + (v0[2] * v0[2] + v0[3] * v0[3]) + (v1[0] * v1[0] + v1[1] * v1[1]) + (v1[2] * v1[2] + v1[3] * v1[3]);
;                         s += __shfl_xor(s, 16); s += __shfl_xor(s, 32);
;                         const int head = (u.pn & 3) * 2 + bj;
;                         if (fq == 0) ssq[(size_t)((kind * 8 + head) * 4 + wc) * MT + row] = s;
;                     } else if (kind <= 3) {
;                         const int i0 = (c0 & 127) >> 1;
;                         const f32x4 csa = *(const f32x4*)(cs + (size_t)pos * 64 + i0), csb = *(const f32x4*)(cs + (size_t)pos * 64 + i0 + 2);
;                         const float sc = (kind == 3) ? KSCALE : 1.0f;
;                         f32x4 w0, w1;
;                         w0[0] = (v0[0] * csa[0] - v0[1] * csa[1]) * sc; w0[1] = (v0[1] * csa[0] + v0[0] * csa[1]) * sc;
;                         w0[2] = (v0[2] * csa[2] - v0[3] * csa[3]) * sc; w0[3] = (v0[3] * csa[2] + v0[2] * csa[3]) * sc;
;                         w1[0] = (v1[0] * csb[0] - v1[1] * csb[1]) * sc; w1[1] = (v1[1] * csb[0] + v1[0] * csb[1]) * sc;
;                         w1[2] = (v1[2] * csb[2] - v1[3] * csb[3]) * sc; w1[3] = (v1[3] * csb[2] + v1[2] * csb[3]) * sc;
;                         v0 = w0; v1 = w1;
;                     } else {
; #pragma unroll
;                         for (int j = 0; j < 4; ++j) { v0[j] = v0[j] * __builtin_amdgcn_rcpf(1.0f + __builtin_amdgcn_exp2f(-1.4426950408889634f * v0[j]));
;                                                       v1[j] = v1[j] * __builtin_amdgcn_rcpf(1.0f + __builtin_amdgcn_exp2f(-1.4426950408889634f * v1[j])); }
.LBB0_226:
	v_lshl_add_u32 v142, s38, 8, v159
	v_readlane_b32 s56, v250, 22
	v_ashrrev_i32_e32 v143, 31, v142
	v_readlane_b32 s57, v250, 23
	s_ashr_i32 s4, s66, 2
	s_cmp_gt_i32 s4, 1
	v_lshl_add_u64 v[146:147], v[142:143], 2, s[56:57]
	global_load_dword v148, v[146:147], off
	global_load_dword v226, v[146:147], off offset:64
	global_load_dword v227, v[146:147], off offset:128
	global_load_dword v228, v[146:147], off offset:192
	global_load_dword v229, v[146:147], off offset:512
	global_load_dword v230, v[146:147], off offset:576
	global_load_dword v231, v[146:147], off offset:640
	global_load_dword v232, v[146:147], off offset:704
	s_cselect_b64 s[0:1], -1, 0
	s_cmp_gt_u32 s4, 3
	s_cselect_b64 s[8:9], -1, 0
	s_cmp_eq_u32 s4, 3
	v_lshlrev_b32_e32 v149, 6, v142
	s_cselect_b64 vcc, -1, 0
	v_and_b32_e32 v163, 0x1f3c0, v149
	v_cndmask_b32_e32 v144, 1.0, v220, vcc
	s_mov_b64 s[2:3], -1
	s_and_b64 vcc, exec, s[0:1]
	s_waitcnt vmcnt(0)
	v_pk_mul_f32 v[126:127], v[126:127], v[148:149] op_sel_hi:[1,0]
	v_pk_mul_f32 v[124:125], v[124:125], v[148:149] op_sel_hi:[1,0]
	v_pk_mul_f32 v[122:123], v[122:123], v[148:149] op_sel_hi:[1,0]
	v_pk_mul_f32 v[120:121], v[120:121], v[148:149] op_sel_hi:[1,0]
	v_cndmask_b32_e64 v149, 0, 1, s[8:9]
	v_cmp_ne_u32_e64 s[38:39], 1, v149
	s_cbranch_vccz .LBB0_232
	s_and_b64 vcc, exec, s[38:39]
	s_cbranch_vccnz .LBB0_229
	v_mul_f32_e32 v149, 0xbfb8aa3b, v124
	v_exp_f32_e32 v149, v149
	v_mul_f32_e32 v150, 0xbfb8aa3b, v120
	v_mul_f32_e32 v151, 0xbfb8aa3b, v125
	v_exp_f32_e32 v152, v150
	v_exp_f32_e32 v151, v151
	v_add_f32_e32 v149, 1.0, v149
	v_rcp_f32_e32 v150, v149
	v_add_f32_e32 v149, 1.0, v152
	v_rcp_f32_e32 v154, v149
	v_add_f32_e32 v149, 1.0, v151
	v_mul_f32_e32 v153, 0xbfb8aa3b, v122
	v_rcp_f32_e32 v151, v149
	v_mul_f32_e32 v149, 0xbfb8aa3b, v121
	v_mul_f32_e32 v152, 0xbfb8aa3b, v126
	v_exp_f32_e32 v153, v153
	v_mul_f32_e32 v155, 0xbfb8aa3b, v127
	v_mul_f32_e32 v156, 0xbfb8aa3b, v123
	v_exp_f32_e32 v149, v149
	v_exp_f32_e32 v152, v152
	v_exp_f32_e32 v155, v155
	v_exp_f32_e32 v157, v156
	v_add_f32_e32 v153, 1.0, v153
	v_add_f32_e32 v149, 1.0, v149
	v_add_f32_e32 v152, 1.0, v152
	v_rcp_f32_e32 v156, v153
	v_add_f32_e32 v153, 1.0, v155
	v_add_f32_e32 v155, 1.0, v157
	v_rcp_f32_e32 v152, v152
	v_rcp_f32_e32 v153, v153
	v_rcp_f32_e32 v157, v155
	v_rcp_f32_e32 v155, v149
	v_pk_mul_f32 v[150:151], v[124:125], v[150:151]
	v_pk_mul_f32 v[152:153], v[126:127], v[152:153]
	v_pk_mul_f32 v[156:157], v[122:123], v[156:157]
	v_pk_mul_f32 v[154:155], v[120:121], v[154:155]
	s_mov_b64 s[2:3], 0

;     __device__ __forceinline__ void operator()(const f32x4 (&acc)[2][2][4][2], const Unit& u, int wr, int wc, int fr, int fq) const {
;     ...
;                 const int row = row0 + ai * HALF + m * 16, pos = row & (MS - 1);
;                 const float rs = rstd[row];
; #pragma unroll
;                 for (int bj = 0; bj < 2; ++bj) {
;                     const int c0 = u.pn * BM + bj * HALF + wc * 32 + 8 * fq;
;                     f32x4 v0 = acc[ai][bj][m][0] * rs, v1 = acc[ai][bj][m][1] * rs;
;                     if (kind <= 1) {
;                         float s = (v0[0] * v0[0] + v0[1] * v0[1]) + (v0[2] * v0[2] + v0[3] * v0[3]) + (v1[0] * v1[0] + v1[1] * v1[1]) + (v1[2] * v1[2] + v1[3] * v1[3]);
;                         s += __shfl_xor(s, 16); s += __shfl_xor(s, 32);
;                         const int head = (u.pn & 3) * 2 + bj;
;                         if (fq == 0) ssq[(size_t)((kind * 8 + head) * 4 + wc) * MT + row] = s;
;                     } else if (kind <= 3) {
;                         const int i0 = (c0 & 127) >> 1;
;                         const f32x4 csa = *(const f32x4*)(cs + (size_t)pos * 64 + i0), csb = *(const f32x4*)(cs + (size_t)pos * 64 + i0 + 2);
;                         const float sc = (kind == 3) ? KSCALE : 1.0f;
;                         f32x4 w0, w1;
;                         w0[0] = (v0[0] * csa[0] - v0[1] * csa[1]) * sc; w0[1] = (v0[1] * csa[0] + v0[0] * csa[1]) * sc;
;                         w0[2] = (v0[2] * csa[2] - v0[3] * csa[3]) * sc; w0[3] = (v0[3] * csa[2] + v0[2] * csa[3]) * sc;
;                         w1[0] = (v1[0] * csb[0] - v1[1] * csb[1]) * sc; w1[1] = (v1[1] * csb[0] + v1[0] * csb[1]) * sc;
;                         w1[2] = (v1[2] * csb[2] - v1[3] * csb[3]) * sc; w1[3] = (v1[3] * csb[2] + v1[2] * csb[3]) * sc;
;                         v0 = w0; v1 = w1;
;                     } else {
; #pragma unroll
;                         for (int j = 0; j < 4; ++j) { v0[j] = v0[j] * __builtin_amdgcn_rcpf(1.0f + __builtin_amdgcn_exp2f(-1.4426950408889634f * v0[j]));
;                                                       v1[j] = v1[j] * __builtin_amdgcn_rcpf(1.0f + __builtin_amdgcn_exp2f(-1.4426950408889634f * v1[j])); }
;                     }
;                     u32x4 w; w.x = cvt_pk_bf16(v0[0], v0[1]); w.y = cvt_pk_bf16(v0[2], v0[3]); w.z = cvt_pk_bf16(v1[0], v1[1]); w.w = cvt_pk_bf16(v1[2], v1[3]);
.LBB0_246:
	v_cvt_pk_bf16_f32 v112, v124, v125
	v_cvt_pk_bf16_f32 v113, v126, v127
	v_cvt_pk_bf16_f32 v114, v148, v149
	v_cvt_pk_bf16_f32 v115, v150, v151
	global_store_dwordx4 v[122:123], v[112:115], off offset:256
	s_and_b64 vcc, exec, s[40:41]
	s_mov_b64 s[0:1], -1
	v_or_b32_e32 v114, 16, v142
	v_ashrrev_i32_e32 v115, 31, v114
	v_lshl_add_u64 v[112:113], v[114:115], 2, s[56:57]
	s_nop 1
	v_mov_b32_e32 v112, v226
	v_lshlrev_b32_e32 v113, 6, v114
	v_and_b32_e32 v115, 0x1f7c0, v113
	v_pk_mul_f32 v[110:111], v[110:111], v[112:113] op_sel_hi:[1,0]
	v_pk_mul_f32 v[108:109], v[108:109], v[112:113] op_sel_hi:[1,0]
	v_pk_mul_f32 v[106:107], v[106:107], v[112:113] op_sel_hi:[1,0]
	v_pk_mul_f32 v[104:105], v[104:105], v[112:113] op_sel_hi:[1,0]
	s_cbranch_vccnz .LBB0_252
	s_and_b64 vcc, exec, s[38:39]
	s_cbranch_vccnz .LBB0_249
	v_mul_f32_e32 v113, 0xbfb8aa3b, v108
	v_exp_f32_e32 v113, v113
	v_mul_f32_e32 v116, 0xbfb8aa3b, v104
	v_mul_f32_e32 v117, 0xbfb8aa3b, v109
	v_exp_f32_e32 v118, v116
	v_exp_f32_e32 v117, v117
	v_add_f32_e32 v113, 1.0, v113
	v_rcp_f32_e32 v116, v113
	v_add_f32_e32 v113, 1.0, v118
	v_rcp_f32_e32 v122, v113
	v_add_f32_e32 v113, 1.0, v117
	v_mul_f32_e32 v119, 0xbfb8aa3b, v106
	v_rcp_f32_e32 v117, v113
	v_mul_f32_e32 v113, 0xbfb8aa3b, v105
	v_mul_f32_e32 v118, 0xbfb8aa3b, v110
	v_exp_f32_e32 v119, v119
	v_mul_f32_e32 v123, 0xbfb8aa3b, v111
	v_mul_f32_e32 v124, 0xbfb8aa3b, v107
	v_exp_f32_e32 v113, v113
	v_exp_f32_e32 v118, v118
	v_exp_f32_e32 v123, v123
	v_exp_f32_e32 v125, v124
	v_add_f32_e32 v119, 1.0, v119
	v_add_f32_e32 v113, 1.0, v113
	v_add_f32_e32 v118, 1.0, v118
	v_rcp_f32_e32 v124, v119
	v_add_f32_e32 v119, 1.0, v123
	v_add_f32_e32 v123, 1.0, v125
	v_rcp_f32_e32 v118, v118
	v_rcp_f32_e32 v119, v119
	v_rcp_f32_e32 v125, v123
	v_rcp_f32_e32 v123, v113
	v_pk_mul_f32 v[116:117], v[108:109], v[116:117]
	v_pk_mul_f32 v[118:119], v[110:111], v[118:119]
	v_pk_mul_f32 v[124:125], v[106:107], v[124:125]
	v_pk_mul_f32 v[122:123], v[104:105], v[122:123]
	s_mov_b64 s[0:1], 0

;     __device__ __forceinline__ void operator()(const f32x4 (&acc)[2][2][4][2], const Unit& u, int wr, int wc, int fr, int fq) const {
;     ...
;                 const int row = row0 + ai * HALF + m * 16, pos = row & (MS - 1);
;                 const float rs = rstd[row];
; #pragma unroll
;                 for (int bj = 0; bj < 2; ++bj) {
;                     const int c0 = u.pn * BM + bj * HALF + wc * 32 + 8 * fq;
;                     f32x4 v0 = acc[ai][bj][m][0] * rs, v1 = acc[ai][bj][m][1] * rs;
;                     if (kind <= 1) {
;                         float s = (v0[0] * v0[0] + v0[1] * v0[1]) + (v0[2] * v0[2] + v0[3] * v0[3]) + (v1[0] * v1[0] + v1[1] * v1[1]) + (v1[2] * v1[2] + v1[3] * v1[3]);
;                         s += __shfl_xor(s, 16); s += __shfl_xor(s, 32);
;                         const int head = (u.pn & 3) * 2 + bj;
;                         if (fq == 0) ssq[(size_t)((kind * 8 + head) * 4 + wc) * MT + row] = s;
;                     } else if (kind <= 3) {
;                         const int i0 = (c0 & 127) >> 1;
;                         const f32x4 csa = *(const f32x4*)(cs + (size_t)pos * 64 + i0), csb = *(const f32x4*)(cs + (size_t)pos * 64 + i0 + 2);
;                         const float sc = (kind == 3) ? KSCALE : 1.0f;
;                         f32x4 w0, w1;
;                         w0[0] = (v0[0] * csa[0] - v0[1] * csa[1]) * sc; w0[1] = (v0[1] * csa[0] + v0[0] * csa[1]) * sc;
;                         w0[2] = (v0[2] * csa[2] - v0[3] * csa[3]) * sc; w0[3] = (v0[3] * csa[2] + v0[2] * csa[3]) * sc;
;                         w1[0] = (v1[0] * csb[0] - v1[1] * csb[1]) * sc; w1[1] = (v1[1] * csb[0] + v1[0] * csb[1]) * sc;
;                         w1[2] = (v1[2] * csb[2] - v1[3] * csb[3]) * sc; w1[3] = (v1[3] * csb[2] + v1[2] * csb[3]) * sc;
;                         v0 = w0; v1 = w1;
;                     } else {
; #pragma unroll
;                         for (int j = 0; j < 4; ++j) { v0[j] = v0[j] * __builtin_amdgcn_rcpf(1.0f + __builtin_amdgcn_exp2f(-1.4426950408889634f * v0[j]));
;                                                       v1[j] = v1[j] * __builtin_amdgcn_rcpf(1.0f + __builtin_amdgcn_exp2f(-1.4426950408889634f * v1[j])); }
;                     }
;                     u32x4 w; w.x = cvt_pk_bf16(v0[0], v0[1]); w.y = cvt_pk_bf16(v0[2], v0[3]); w.z = cvt_pk_bf16(v1[0], v1[1]); w.w = cvt_pk_bf16(v1[2], v1[3]);
.LBB0_266:
	v_cvt_pk_bf16_f32 v96, v106, v107
	v_cvt_pk_bf16_f32 v97, v108, v109
	v_cvt_pk_bf16_f32 v98, v110, v111
	v_cvt_pk_bf16_f32 v99, v112, v113
	global_store_dwordx4 v[104:105], v[96:99], off offset:256
	s_and_b64 vcc, exec, s[40:41]
	s_mov_b64 s[0:1], -1
	v_or_b32_e32 v98, 32, v142
	v_ashrrev_i32_e32 v99, 31, v98
	v_lshl_add_u64 v[96:97], v[98:99], 2, s[56:57]
	s_nop 1
	v_mov_b32_e32 v96, v227
	v_lshlrev_b32_e32 v97, 6, v98
	v_and_b32_e32 v99, 0x1fbc0, v97
	v_pk_mul_f32 v[94:95], v[94:95], v[96:97] op_sel_hi:[1,0]
	v_pk_mul_f32 v[92:93], v[92:93], v[96:97] op_sel_hi:[1,0]
	v_pk_mul_f32 v[90:91], v[90:91], v[96:97] op_sel_hi:[1,0]
	v_pk_mul_f32 v[88:89], v[88:89], v[96:97] op_sel_hi:[1,0]
	s_cbranch_vccnz .LBB0_272
	s_and_b64 vcc, exec, s[38:39]
	s_cbranch_vccnz .LBB0_269
	v_mul_f32_e32 v97, 0xbfb8aa3b, v92
	v_exp_f32_e32 v97, v97
	v_mul_f32_e32 v100, 0xbfb8aa3b, v88
	v_mul_f32_e32 v101, 0xbfb8aa3b, v93
	v_exp_f32_e32 v102, v100
	v_exp_f32_e32 v101, v101
	v_add_f32_e32 v97, 1.0, v97
	v_rcp_f32_e32 v100, v97
	v_add_f32_e32 v97, 1.0, v102
	v_rcp_f32_e32 v104, v97
	v_add_f32_e32 v97, 1.0, v101
	v_mul_f32_e32 v103, 0xbfb8aa3b, v90
	v_rcp_f32_e32 v101, v97
	v_mul_f32_e32 v97, 0xbfb8aa3b, v89
	v_mul_f32_e32 v102, 0xbfb8aa3b, v94
	v_exp_f32_e32 v103, v103
	v_mul_f32_e32 v105, 0xbfb8aa3b, v95
	v_mul_f32_e32 v106, 0xbfb8aa3b, v91
	v_exp_f32_e32 v97, v97
	v_exp_f32_e32 v102, v102
	v_exp_f32_e32 v105, v105
	v_exp_f32_e32 v107, v106
	v_add_f32_e32 v103, 1.0, v103
	v_add_f32_e32 v97, 1.0, v97
	v_add_f32_e32 v102, 1.0, v102
	v_rcp_f32_e32 v106, v103
	v_add_f32_e32 v103, 1.0, v105
	v_add_f32_e32 v105, 1.0, v107
	v_rcp_f32_e32 v102, v102
	v_rcp_f32_e32 v103, v103
	v_rcp_f32_e32 v107, v105
	v_rcp_f32_e32 v105, v97
	v_pk_mul_f32 v[100:101], v[92:93], v[100:101]
	v_pk_mul_f32 v[102:103], v[94:95], v[102:103]
	v_pk_mul_f32 v[106:107], v[90:91], v[106:107]
	v_pk_mul_f32 v[104:105], v[88:89], v[104:105]
	s_mov_b64 s[0:1], 0

;     __device__ __forceinline__ void operator()(const f32x4 (&acc)[2][2][4][2], const Unit& u, int wr, int wc, int fr, int fq) const {
;     ...
;                 const int row = row0 + ai * HALF + m * 16, pos = row & (MS - 1);
;                 const float rs = rstd[row];
; #pragma unroll
;                 for (int bj = 0; bj < 2; ++bj) {
;                     const int c0 = u.pn * BM + bj * HALF + wc * 32 + 8 * fq;
;                     f32x4 v0 = acc[ai][bj][m][0] * rs, v1 = acc[ai][bj][m][1] * rs;
;                     if (kind <= 1) {
;                         float s = (v0[0] * v0[0] + v0[1] * v0[1]) + (v0[2] * v0[2] + v0[3] * v0[3]) + (v1[0] * v1[0] + v1[1] * v1[1]) + (v1[2] * v1[2] + v1[3] * v1[3]);
;                         s += __shfl_xor(s, 16); s += __shfl_xor(s, 32);
;                         const int head = (u.pn & 3) * 2 + bj;
;                         if (fq == 0) ssq[(size_t)((kind * 8 + head) * 4 + wc) * MT + row] = s;
;                     } else if (kind <= 3) {
;                         const int i0 = (c0 & 127) >> 1;
;                         const f32x4 csa = *(const f32x4*)(cs + (size_t)pos * 64 + i0), csb = *(const f32x4*)(cs + (size_t)pos * 64 + i0 + 2);
;                         const float sc = (kind == 3) ? KSCALE : 1.0f;
;                         f32x4 w0, w1;
;                         w0[0] = (v0[0] * csa[0] - v0[1] * csa[1]) * sc; w0[1] = (v0[1] * csa[0] + v0[0] * csa[1]) * sc;
;                         w0[2] = (v0[2] * csa[2] - v0[3] * csa[3]) * sc; w0[3] = (v0[3] * csa[2] + v0[2] * csa[3]) * sc;
;                         w1[0] = (v1[0] * csb[0] - v1[1] * csb[1]) * sc; w1[1] = (v1[1] * csb[0] + v1[0] * csb[1]) * sc;
;                         w1[2] = (v1[2] * csb[2] - v1[3] * csb[3]) * sc; w1[3] = (v1[3] * csb[2] + v1[2] * csb[3]) * sc;
;                         v0 = w0; v1 = w1;
;                     } else {
; #pragma unroll
;                         for (int j = 0; j < 4; ++j) { v0[j] = v0[j] * __builtin_amdgcn_rcpf(1.0f + __builtin_amdgcn_exp2f(-1.4426950408889634f * v0[j]));
;                                                       v1[j] = v1[j] * __builtin_amdgcn_rcpf(1.0f + __builtin_amdgcn_exp2f(-1.4426950408889634f * v1[j])); }
;                     }
;                     u32x4 w; w.x = cvt_pk_bf16(v0[0], v0[1]); w.y = cvt_pk_bf16(v0[2], v0[3]); w.z = cvt_pk_bf16(v1[0], v1[1]); w.w = cvt_pk_bf16(v1[2], v1[3]);
.LBB0_286:
	v_cvt_pk_bf16_f32 v80, v90, v91
	v_cvt_pk_bf16_f32 v81, v92, v93
	v_cvt_pk_bf16_f32 v82, v94, v95
	v_cvt_pk_bf16_f32 v83, v96, v97
	global_store_dwordx4 v[88:89], v[80:83], off offset:256
	s_and_b64 vcc, exec, s[40:41]
	s_mov_b64 s[0:1], -1
	v_or_b32_e32 v82, 48, v142
	v_ashrrev_i32_e32 v83, 31, v82
	v_lshl_add_u64 v[80:81], v[82:83], 2, s[56:57]
	s_nop 1
	v_mov_b32_e32 v80, v228
	v_lshlrev_b32_e32 v81, 6, v82
	v_and_b32_e32 v83, 0x1ffc0, v81
	v_pk_mul_f32 v[78:79], v[78:79], v[80:81] op_sel_hi:[1,0]
	v_pk_mul_f32 v[76:77], v[76:77], v[80:81] op_sel_hi:[1,0]
	v_pk_mul_f32 v[74:75], v[74:75], v[80:81] op_sel_hi:[1,0]
	v_pk_mul_f32 v[72:73], v[72:73], v[80:81] op_sel_hi:[1,0]
	s_cbranch_vccnz .LBB0_292
	s_and_b64 vcc, exec, s[38:39]
	s_cbranch_vccnz .LBB0_289
	v_mul_f32_e32 v81, 0xbfb8aa3b, v76
	v_exp_f32_e32 v81, v81
	v_mul_f32_e32 v84, 0xbfb8aa3b, v72
	v_mul_f32_e32 v85, 0xbfb8aa3b, v77
	v_exp_f32_e32 v86, v84
	v_exp_f32_e32 v85, v85
	v_add_f32_e32 v81, 1.0, v81
	v_rcp_f32_e32 v84, v81
	v_add_f32_e32 v81, 1.0, v86
	v_rcp_f32_e32 v88, v81
	v_add_f32_e32 v81, 1.0, v85
	v_mul_f32_e32 v87, 0xbfb8aa3b, v74
	v_rcp_f32_e32 v85, v81
	v_mul_f32_e32 v81, 0xbfb8aa3b, v73
	v_mul_f32_e32 v86, 0xbfb8aa3b, v78
	v_exp_f32_e32 v87, v87
	v_mul_f32_e32 v89, 0xbfb8aa3b, v79
	v_mul_f32_e32 v90, 0xbfb8aa3b, v75
	v_exp_f32_e32 v81, v81
	v_exp_f32_e32 v86, v86
	v_exp_f32_e32 v89, v89
	v_exp_f32_e32 v91, v90
	v_add_f32_e32 v87, 1.0, v87
	v_add_f32_e32 v81, 1.0, v81
	v_add_f32_e32 v86, 1.0, v86
	v_rcp_f32_e32 v90, v87
	v_add_f32_e32 v87, 1.0, v89
	v_add_f32_e32 v89, 1.0, v91
	v_rcp_f32_e32 v86, v86
	v_rcp_f32_e32 v87, v87
	v_rcp_f32_e32 v91, v89
	v_rcp_f32_e32 v89, v81
	v_pk_mul_f32 v[84:85], v[76:77], v[84:85]
	v_pk_mul_f32 v[86:87], v[78:79], v[86:87]
	v_pk_mul_f32 v[90:91], v[74:75], v[90:91]
	v_pk_mul_f32 v[88:89], v[72:73], v[88:89]
	s_mov_b64 s[0:1], 0

;     __device__ __forceinline__ void operator()(const f32x4 (&acc)[2][2][4][2], const Unit& u, int wr, int wc, int fr, int fq) const {
;     ...
;                 const int row = row0 + ai * HALF + m * 16, pos = row & (MS - 1);
;                 const float rs = rstd[row];
; #pragma unroll
;                 for (int bj = 0; bj < 2; ++bj) {
;                     const int c0 = u.pn * BM + bj * HALF + wc * 32 + 8 * fq;
;                     f32x4 v0 = acc[ai][bj][m][0] * rs, v1 = acc[ai][bj][m][1] * rs;
;                     if (kind <= 1) {
;                         float s = (v0[0] * v0[0] + v0[1] * v0[1]) + (v0[2] * v0[2] + v0[3] * v0[3]) + (v1[0] * v1[0] + v1[1] * v1[1]) + (v1[2] * v1[2] + v1[3] * v1[3]);
;                         s += __shfl_xor(s, 16); s += __shfl_xor(s, 32);
;                         const int head = (u.pn & 3) * 2 + bj;
;                         if (fq == 0) ssq[(size_t)((kind * 8 + head) * 4 + wc) * MT + row] = s;
;                     } else if (kind <= 3) {
;                         const int i0 = (c0 & 127) >> 1;
;                         const f32x4 csa = *(const f32x4*)(cs + (size_t)pos * 64 + i0), csb = *(const f32x4*)(cs + (size_t)pos * 64 + i0 + 2);
;                         const float sc = (kind == 3) ? KSCALE : 1.0f;
;                         f32x4 w0, w1;
;                         w0[0] = (v0[0] * csa[0] - v0[1] * csa[1]) * sc; w0[1] = (v0[1] * csa[0] + v0[0] * csa[1]) * sc;
;                         w0[2] = (v0[2] * csa[2] - v0[3] * csa[3]) * sc; w0[3] = (v0[3] * csa[2] + v0[2] * csa[3]) * sc;
;                         w1[0] = (v1[0] * csb[0] - v1[1] * csb[1]) * sc; w1[1] = (v1[1] * csb[0] + v1[0] * csb[1]) * sc;
;                         w1[2] = (v1[2] * csb[2] - v1[3] * csb[3]) * sc; w1[3] = (v1[3] * csb[2] + v1[2] * csb[3]) * sc;
;                         v0 = w0; v1 = w1;
;                     } else {
; #pragma unroll
;                         for (int j = 0; j < 4; ++j) { v0[j] = v0[j] * __builtin_amdgcn_rcpf(1.0f + __builtin_amdgcn_exp2f(-1.4426950408889634f * v0[j]));
;                                                       v1[j] = v1[j] * __builtin_amdgcn_rcpf(1.0f + __builtin_amdgcn_exp2f(-1.4426950408889634f * v1[j])); }
;                     }
;                     u32x4 w; w.x = cvt_pk_bf16(v0[0], v0[1]); w.y = cvt_pk_bf16(v0[2], v0[3]); w.z = cvt_pk_bf16(v1[0], v1[1]); w.w = cvt_pk_bf16(v1[2], v1[3]);
.LBB0_306:
	v_cvt_pk_bf16_f32 v64, v74, v75
	v_cvt_pk_bf16_f32 v65, v76, v77
	v_cvt_pk_bf16_f32 v66, v78, v79
	v_cvt_pk_bf16_f32 v67, v80, v81
	global_store_dwordx4 v[72:73], v[64:67], off offset:256
	s_nop 1
	v_mov_b32_e32 v64, v229
	v_add_u32_e32 v75, 0x80, v142
	v_lshlrev_b32_e32 v65, 6, v75
	s_and_b64 vcc, exec, s[40:41]
	v_and_b32_e32 v74, 0x1f3c0, v65
	s_mov_b64 s[0:1], -1
	v_pk_mul_f32 v[62:63], v[62:63], v[64:65] op_sel_hi:[1,0]
	v_pk_mul_f32 v[60:61], v[60:61], v[64:65] op_sel_hi:[1,0]
	v_pk_mul_f32 v[58:59], v[58:59], v[64:65] op_sel_hi:[1,0]
	v_pk_mul_f32 v[56:57], v[56:57], v[64:65] op_sel_hi:[1,0]
	s_cbranch_vccnz .LBB0_312
	s_and_b64 vcc, exec, s[38:39]
	s_cbranch_vccnz .LBB0_309
	v_mul_f32_e32 v65, 0xbfb8aa3b, v60
	v_exp_f32_e32 v65, v65
	v_mul_f32_e32 v66, 0xbfb8aa3b, v56
	v_mul_f32_e32 v67, 0xbfb8aa3b, v61
	v_exp_f32_e32 v68, v66
	v_exp_f32_e32 v67, v67
	v_add_f32_e32 v65, 1.0, v65
	v_rcp_f32_e32 v66, v65
	v_add_f32_e32 v65, 1.0, v68
	v_rcp_f32_e32 v70, v65
	v_add_f32_e32 v65, 1.0, v67
	v_mul_f32_e32 v69, 0xbfb8aa3b, v58
	v_rcp_f32_e32 v67, v65
	v_mul_f32_e32 v65, 0xbfb8aa3b, v57
	v_mul_f32_e32 v68, 0xbfb8aa3b, v62
	v_exp_f32_e32 v69, v69
	v_mul_f32_e32 v71, 0xbfb8aa3b, v63
	v_mul_f32_e32 v72, 0xbfb8aa3b, v59
	v_exp_f32_e32 v65, v65
	v_exp_f32_e32 v68, v68
	v_exp_f32_e32 v71, v71
	v_exp_f32_e32 v73, v72
	v_add_f32_e32 v69, 1.0, v69
	v_add_f32_e32 v65, 1.0, v65
	v_add_f32_e32 v68, 1.0, v68
	v_rcp_f32_e32 v72, v69
	v_add_f32_e32 v69, 1.0, v71
	v_add_f32_e32 v71, 1.0, v73
	v_rcp_f32_e32 v68, v68
	v_rcp_f32_e32 v69, v69
	v_rcp_f32_e32 v73, v71
	v_rcp_f32_e32 v71, v65
	v_pk_mul_f32 v[66:67], v[60:61], v[66:67]
	v_pk_mul_f32 v[68:69], v[62:63], v[68:69]
	v_pk_mul_f32 v[72:73], v[58:59], v[72:73]
	v_pk_mul_f32 v[70:71], v[56:57], v[70:71]
	s_mov_b64 s[0:1], 0

;     __device__ __forceinline__ void operator()(const f32x4 (&acc)[2][2][4][2], const Unit& u, int wr, int wc, int fr, int fq) const {
;     ...
;                 const int row = row0 + ai * HALF + m * 16, pos = row & (MS - 1);
;                 const float rs = rstd[row];
; #pragma unroll
;                 for (int bj = 0; bj < 2; ++bj) {
;                     const int c0 = u.pn * BM + bj * HALF + wc * 32 + 8 * fq;
;                     f32x4 v0 = acc[ai][bj][m][0] * rs, v1 = acc[ai][bj][m][1] * rs;
;                     if (kind <= 1) {
;                         float s = (v0[0] * v0[0] + v0[1] * v0[1]) + (v0[2] * v0[2] + v0[3] * v0[3]) + (v1[0] * v1[0] + v1[1] * v1[1]) + (v1[2] * v1[2] + v1[3] * v1[3]);
;                         s += __shfl_xor(s, 16); s += __shfl_xor(s, 32);
;                         const int head = (u.pn & 3) * 2 + bj;
;                         if (fq == 0) ssq[(size_t)((kind * 8 + head) * 4 + wc) * MT + row] = s;
;                     } else if (kind <= 3) {
;                         const int i0 = (c0 & 127) >> 1;
;                         const f32x4 csa = *(const f32x4*)(cs + (size_t)pos * 64 + i0), csb = *(const f32x4*)(cs + (size_t)pos * 64 + i0 + 2);
;                         const float sc = (kind == 3) ? KSCALE : 1.0f;
;                         f32x4 w0, w1;
;                         w0[0] = (v0[0] * csa[0] - v0[1] * csa[1]) * sc; w0[1] = (v0[1] * csa[0] + v0[0] * csa[1]) * sc;
;                         w0[2] = (v0[2] * csa[2] - v0[3] * csa[3]) * sc; w0[3] = (v0[3] * csa[2] + v0[2] * csa[3]) * sc;
;                         w1[0] = (v1[0] * csb[0] - v1[1] * csb[1]) * sc; w1[1] = (v1[1] * csb[0] + v1[0] * csb[1]) * sc;
;                         w1[2] = (v1[2] * csb[2] - v1[3] * csb[3]) * sc; w1[3] = (v1[3] * csb[2] + v1[2] * csb[3]) * sc;
;                         v0 = w0; v1 = w1;
;                     } else {
; #pragma unroll
;                         for (int j = 0; j < 4; ++j) { v0[j] = v0[j] * __builtin_amdgcn_rcpf(1.0f + __builtin_amdgcn_exp2f(-1.4426950408889634f * v0[j]));
;                                                       v1[j] = v1[j] * __builtin_amdgcn_rcpf(1.0f + __builtin_amdgcn_exp2f(-1.4426950408889634f * v1[j])); }
;                     }
;                     u32x4 w; w.x = cvt_pk_bf16(v0[0], v0[1]); w.y = cvt_pk_bf16(v0[2], v0[3]); w.z = cvt_pk_bf16(v1[0], v1[1]); w.w = cvt_pk_bf16(v1[2], v1[3]);
.LBB0_326:
	v_cvt_pk_bf16_f32 v48, v58, v59
	v_cvt_pk_bf16_f32 v49, v60, v61
	v_cvt_pk_bf16_f32 v50, v62, v63
	v_cvt_pk_bf16_f32 v51, v64, v65
	global_store_dwordx4 v[56:57], v[48:51], off offset:256
	s_nop 1
	v_mov_b32_e32 v48, v230
	v_add_u32_e32 v59, 0x90, v142
	v_lshlrev_b32_e32 v49, 6, v59
	s_and_b64 vcc, exec, s[40:41]
	v_and_b32_e32 v58, 0x1f7c0, v49
	s_mov_b64 s[0:1], -1
	v_pk_mul_f32 v[46:47], v[46:47], v[48:49] op_sel_hi:[1,0]
	v_pk_mul_f32 v[44:45], v[44:45], v[48:49] op_sel_hi:[1,0]
	v_pk_mul_f32 v[42:43], v[42:43], v[48:49] op_sel_hi:[1,0]
	v_pk_mul_f32 v[40:41], v[40:41], v[48:49] op_sel_hi:[1,0]
	s_cbranch_vccnz .LBB0_332
	s_and_b64 vcc, exec, s[38:39]
	s_cbranch_vccnz .LBB0_329
	v_mul_f32_e32 v49, 0xbfb8aa3b, v44
	v_exp_f32_e32 v49, v49
	v_mul_f32_e32 v50, 0xbfb8aa3b, v40
	v_mul_f32_e32 v51, 0xbfb8aa3b, v45
	v_exp_f32_e32 v52, v50
	v_exp_f32_e32 v51, v51
	v_add_f32_e32 v49, 1.0, v49
	v_rcp_f32_e32 v50, v49
	v_add_f32_e32 v49, 1.0, v52
	v_rcp_f32_e32 v54, v49
	v_add_f32_e32 v49, 1.0, v51
	v_mul_f32_e32 v53, 0xbfb8aa3b, v42
	v_rcp_f32_e32 v51, v49
	v_mul_f32_e32 v49, 0xbfb8aa3b, v41
	v_mul_f32_e32 v52, 0xbfb8aa3b, v46
	v_exp_f32_e32 v53, v53
	v_mul_f32_e32 v55, 0xbfb8aa3b, v47
	v_mul_f32_e32 v56, 0xbfb8aa3b, v43
	v_exp_f32_e32 v49, v49
	v_exp_f32_e32 v52, v52
	v_exp_f32_e32 v55, v55
	v_exp_f32_e32 v57, v56
	v_add_f32_e32 v53, 1.0, v53
	v_add_f32_e32 v49, 1.0, v49
	v_add_f32_e32 v52, 1.0, v52
	v_rcp_f32_e32 v56, v53
	v_add_f32_e32 v53, 1.0, v55
	v_add_f32_e32 v55, 1.0, v57
	v_rcp_f32_e32 v52, v52
	v_rcp_f32_e32 v53, v53
	v_rcp_f32_e32 v57, v55
	v_rcp_f32_e32 v55, v49
	v_pk_mul_f32 v[50:51], v[44:45], v[50:51]
	v_pk_mul_f32 v[52:53], v[46:47], v[52:53]
	v_pk_mul_f32 v[56:57], v[42:43], v[56:57]
	v_pk_mul_f32 v[54:55], v[40:41], v[54:55]
	s_mov_b64 s[0:1], 0

;     __device__ __forceinline__ void operator()(const f32x4 (&acc)[2][2][4][2], const Unit& u, int wr, int wc, int fr, int fq) const {
;     ...
;                 const int row = row0 + ai * HALF + m * 16, pos = row & (MS - 1);
;                 const float rs = rstd[row];
; #pragma unroll
;                 for (int bj = 0; bj < 2; ++bj) {
;                     const int c0 = u.pn * BM + bj * HALF + wc * 32 + 8 * fq;
;                     f32x4 v0 = acc[ai][bj][m][0] * rs, v1 = acc[ai][bj][m][1] * rs;
;                     if (kind <= 1) {
;                         float s = (v0[0] * v0[0] + v0[1] * v0[1]) + (v0[2] * v0[2] + v0[3] * v0[3]) + (v1[0] * v1[0] + v1[1] * v1[1]) + (v1[2] * v1[2] + v1[3] * v1[3]);
;                         s += __shfl_xor(s, 16); s += __shfl_xor(s, 32);
;                         const int head = (u.pn & 3) * 2 + bj;
;                         if (fq == 0) ssq[(size_t)((kind * 8 + head) * 4 + wc) * MT + row] = s;
;                     } else if (kind <= 3) {
;                         const int i0 = (c0 & 127) >> 1;
;                         const f32x4 csa = *(const f32x4*)(cs + (size_t)pos * 64 + i0), csb = *(const f32x4*)(cs + (size_t)pos * 64 + i0 + 2);
;                         const float sc = (kind == 3) ? KSCALE : 1.0f;
;                         f32x4 w0, w1;
;                         w0[0] = (v0[0] * csa[0] - v0[1] * csa[1]) * sc; w0[1] = (v0[1] * csa[0] + v0[0] * csa[1]) * sc;
;                         w0[2] = (v0[2] * csa[2] - v0[3] * csa[3]) * sc; w0[3] = (v0[3] * csa[2] + v0[2] * csa[3]) * sc;
;                         w1[0] = (v1[0] * csb[0] - v1[1] * csb[1]) * sc; w1[1] = (v1[1] * csb[0] + v1[0] * csb[1]) * sc;
;                         w1[2] = (v1[2] * csb[2] - v1[3] * csb[3]) * sc; w1[3] = (v1[3] * csb[2] + v1[2] * csb[3]) * sc;
;                         v0 = w0; v1 = w1;
;                     } else {
; #pragma unroll
;                         for (int j = 0; j < 4; ++j) { v0[j] = v0[j] * __builtin_amdgcn_rcpf(1.0f + __builtin_amdgcn_exp2f(-1.4426950408889634f * v0[j]));
;                                                       v1[j] = v1[j] * __builtin_amdgcn_rcpf(1.0f + __builtin_amdgcn_exp2f(-1.4426950408889634f * v1[j])); }
;                     }
;                     u32x4 w; w.x = cvt_pk_bf16(v0[0], v0[1]); w.y = cvt_pk_bf16(v0[2], v0[3]); w.z = cvt_pk_bf16(v1[0], v1[1]); w.w = cvt_pk_bf16(v1[2], v1[3]);
.LBB0_346:
	v_cvt_pk_bf16_f32 v32, v42, v43
	v_cvt_pk_bf16_f32 v33, v44, v45
	v_cvt_pk_bf16_f32 v34, v46, v47
	v_cvt_pk_bf16_f32 v35, v48, v49
	global_store_dwordx4 v[40:41], v[32:35], off offset:256
	s_nop 1
	v_mov_b32_e32 v32, v231
	v_add_u32_e32 v43, 0xa0, v142
	v_lshlrev_b32_e32 v33, 6, v43
	s_and_b64 vcc, exec, s[40:41]
	v_and_b32_e32 v42, 0x1fbc0, v33
	s_mov_b64 s[0:1], -1
	v_pk_mul_f32 v[30:31], v[30:31], v[32:33] op_sel_hi:[1,0]
	v_pk_mul_f32 v[28:29], v[28:29], v[32:33] op_sel_hi:[1,0]
	v_pk_mul_f32 v[26:27], v[26:27], v[32:33] op_sel_hi:[1,0]
	v_pk_mul_f32 v[24:25], v[24:25], v[32:33] op_sel_hi:[1,0]
	s_cbranch_vccnz .LBB0_352
	s_and_b64 vcc, exec, s[38:39]
	s_cbranch_vccnz .LBB0_349
	v_mul_f32_e32 v33, 0xbfb8aa3b, v28
	v_exp_f32_e32 v33, v33
	v_mul_f32_e32 v34, 0xbfb8aa3b, v24
	v_mul_f32_e32 v35, 0xbfb8aa3b, v29
	v_exp_f32_e32 v36, v34
	v_exp_f32_e32 v35, v35
	v_add_f32_e32 v33, 1.0, v33
	v_rcp_f32_e32 v34, v33
	v_add_f32_e32 v33, 1.0, v36
	v_rcp_f32_e32 v38, v33
	v_add_f32_e32 v33, 1.0, v35
	v_mul_f32_e32 v37, 0xbfb8aa3b, v26
	v_rcp_f32_e32 v35, v33
	v_mul_f32_e32 v33, 0xbfb8aa3b, v25
	v_mul_f32_e32 v36, 0xbfb8aa3b, v30
	v_exp_f32_e32 v37, v37
	v_mul_f32_e32 v39, 0xbfb8aa3b, v31
	v_mul_f32_e32 v40, 0xbfb8aa3b, v27
	v_exp_f32_e32 v33, v33
	v_exp_f32_e32 v36, v36
	v_exp_f32_e32 v39, v39
	v_exp_f32_e32 v41, v40
	v_add_f32_e32 v37, 1.0, v37
	v_add_f32_e32 v33, 1.0, v33
	v_add_f32_e32 v36, 1.0, v36
	v_rcp_f32_e32 v40, v37
	v_add_f32_e32 v37, 1.0, v39
	v_add_f32_e32 v39, 1.0, v41
	v_rcp_f32_e32 v36, v36
	v_rcp_f32_e32 v37, v37
	v_rcp_f32_e32 v41, v39
	v_rcp_f32_e32 v39, v33
	v_pk_mul_f32 v[34:35], v[28:29], v[34:35]
	v_pk_mul_f32 v[36:37], v[30:31], v[36:37]
	v_pk_mul_f32 v[40:41], v[26:27], v[40:41]
	v_pk_mul_f32 v[38:39], v[24:25], v[38:39]
	s_mov_b64 s[0:1], 0

;     __device__ __forceinline__ void operator()(const f32x4 (&acc)[2][2][4][2], const Unit& u, int wr, int wc, int fr, int fq) const {
;     ...
;                 const int row = row0 + ai * HALF + m * 16, pos = row & (MS - 1);
;                 const float rs = rstd[row];
; #pragma unroll
;                 for (int bj = 0; bj < 2; ++bj) {
;                     const int c0 = u.pn * BM + bj * HALF + wc * 32 + 8 * fq;
;                     f32x4 v0 = acc[ai][bj][m][0] * rs, v1 = acc[ai][bj][m][1] * rs;
;                     if (kind <= 1) {
;                         float s = (v0[0] * v0[0] + v0[1] * v0[1]) + (v0[2] * v0[2] + v0[3] * v0[3]) + (v1[0] * v1[0] + v1[1] * v1[1]) + (v1[2] * v1[2] + v1[3] * v1[3]);
;                         s += __shfl_xor(s, 16); s += __shfl_xor(s, 32);
;                         const int head = (u.pn & 3) * 2 + bj;
;                         if (fq == 0) ssq[(size_t)((kind * 8 + head) * 4 + wc) * MT + row] = s;
;                     } else if (kind <= 3) {
;                         const int i0 = (c0 & 127) >> 1;
;                         const f32x4 csa = *(const f32x4*)(cs + (size_t)pos * 64 + i0), csb = *(const f32x4*)(cs + (size_t)pos * 64 + i0 + 2);
;                         const float sc = (kind == 3) ? KSCALE : 1.0f;
;                         f32x4 w0, w1;
;                         w0[0] = (v0[0] * csa[0] - v0[1] * csa[1]) * sc; w0[1] = (v0[1] * csa[0] + v0[0] * csa[1]) * sc;
;                         w0[2] = (v0[2] * csa[2] - v0[3] * csa[3]) * sc; w0[3] = (v0[3] * csa[2] + v0[2] * csa[3]) * sc;
;                         w1[0] = (v1[0] * csb[0] - v1[1] * csb[1]) * sc; w1[1] = (v1[1] * csb[0] + v1[0] * csb[1]) * sc;
;                         w1[2] = (v1[2] * csb[2] - v1[3] * csb[3]) * sc; w1[3] = (v1[3] * csb[2] + v1[2] * csb[3]) * sc;
;                         v0 = w0; v1 = w1;
;                     } else {
; #pragma unroll
;                         for (int j = 0; j < 4; ++j) { v0[j] = v0[j] * __builtin_amdgcn_rcpf(1.0f + __builtin_amdgcn_exp2f(-1.4426950408889634f * v0[j]));
;                                                       v1[j] = v1[j] * __builtin_amdgcn_rcpf(1.0f + __builtin_amdgcn_exp2f(-1.4426950408889634f * v1[j])); }
;                     }
;                     u32x4 w; w.x = cvt_pk_bf16(v0[0], v0[1]); w.y = cvt_pk_bf16(v0[2], v0[3]); w.z = cvt_pk_bf16(v1[0], v1[1]); w.w = cvt_pk_bf16(v1[2], v1[3]);
.LBB0_366:
	v_cvt_pk_bf16_f32 v16, v26, v27
	v_cvt_pk_bf16_f32 v17, v28, v29
	v_cvt_pk_bf16_f32 v18, v30, v31
	v_cvt_pk_bf16_f32 v19, v32, v33
	global_store_dwordx4 v[24:25], v[16:19], off offset:256
	s_nop 1
	v_mov_b32_e32 v16, v232
	v_add_u32_e32 v27, 0xb0, v142
	v_lshlrev_b32_e32 v17, 6, v27
	s_and_b64 vcc, exec, s[40:41]
	v_and_b32_e32 v26, 0x1ffc0, v17
	s_mov_b64 s[0:1], -1
	v_pk_mul_f32 v[14:15], v[14:15], v[16:17] op_sel_hi:[1,0]
	v_pk_mul_f32 v[12:13], v[12:13], v[16:17] op_sel_hi:[1,0]
	v_pk_mul_f32 v[10:11], v[10:11], v[16:17] op_sel_hi:[1,0]
	v_pk_mul_f32 v[8:9], v[8:9], v[16:17] op_sel_hi:[1,0]
	s_cbranch_vccnz .LBB0_372
	s_and_b64 vcc, exec, s[38:39]
	s_cbranch_vccnz .LBB0_369
	v_mul_f32_e32 v17, 0xbfb8aa3b, v12
	v_exp_f32_e32 v17, v17
	v_mul_f32_e32 v18, 0xbfb8aa3b, v8
	v_mul_f32_e32 v19, 0xbfb8aa3b, v13
	v_exp_f32_e32 v20, v18
	v_exp_f32_e32 v19, v19
	v_add_f32_e32 v17, 1.0, v17
	v_rcp_f32_e32 v18, v17
	v_add_f32_e32 v17, 1.0, v20
	v_rcp_f32_e32 v22, v17
	v_add_f32_e32 v17, 1.0, v19
	v_mul_f32_e32 v21, 0xbfb8aa3b, v10
	v_rcp_f32_e32 v19, v17
	v_mul_f32_e32 v17, 0xbfb8aa3b, v9
	v_mul_f32_e32 v20, 0xbfb8aa3b, v14
	v_exp_f32_e32 v21, v21
	v_mul_f32_e32 v23, 0xbfb8aa3b, v15
	v_mul_f32_e32 v24, 0xbfb8aa3b, v11
	v_exp_f32_e32 v17, v17
	v_exp_f32_e32 v20, v20
	v_exp_f32_e32 v23, v23
	v_exp_f32_e32 v25, v24
	v_add_f32_e32 v21, 1.0, v21
	v_add_f32_e32 v17, 1.0, v17
	v_add_f32_e32 v20, 1.0, v20
	v_rcp_f32_e32 v24, v21
	v_add_f32_e32 v21, 1.0, v23
	v_add_f32_e32 v23, 1.0, v25
	v_rcp_f32_e32 v20, v20
	v_rcp_f32_e32 v21, v21
	v_rcp_f32_e32 v25, v23
	v_rcp_f32_e32 v23, v17
	v_pk_mul_f32 v[18:19], v[12:13], v[18:19]
	v_pk_mul_f32 v[20:21], v[14:15], v[20:21]
	v_pk_mul_f32 v[24:25], v[10:11], v[24:25]
	v_pk_mul_f32 v[22:23], v[8:9], v[22:23]
	s_mov_b64 s[0:1], 0
